# s_barrier at the top of every phase-B block keeps the 8 waves writing the same 16 rows together (full 8 KiB rows)
# speedup vs baseline: 1.0299x; 1.0291x over previous
.LBB0_3:
	s_barrier
	ds_read_b128 v[70:73], v203
	v_add_u32_e32 v132, s12, v220
	s_add_i32 s12, s12, 0x2000000
	v_add_u32_e32 v203, 0x400, v203
	s_cmp_eq_u32 s12, 0x10000000
	s_waitcnt lgkmcnt(0)
	v_mfma_f32_16x16x32_bf16 v[66:69], v[144:147], v[70:73], 0
	v_add_u32_e32 v133, 0x4000, v132
	v_add_u32_e32 v134, 0x8000, v132
	v_add_u32_e32 v135, 0xc000, v132
	v_mfma_f32_16x16x32_bf16 v[74:77], v[148:151], v[70:73], 0
	v_add_u32_e32 v136, 0x10000, v132
	s_nop 2
	v_exp_f32_e32 v66, v66
	v_exp_f32_e32 v67, v67
	v_mfma_f32_16x16x32_bf16 v[78:81], v[152:155], v[70:73], 0
	v_exp_f32_e32 v68, v68
	v_exp_f32_e32 v69, v69
	v_exp_f32_e32 v74, v74
	v_mfma_f32_16x16x32_bf16 v[82:85], v[156:159], v[70:73], 0
	v_exp_f32_e32 v75, v75
	v_exp_f32_e32 v76, v76
	v_exp_f32_e32 v77, v77
	v_mfma_f32_16x16x32_bf16 v[86:89], v[160:163], v[70:73], 0
	v_exp_f32_e32 v78, v78
	v_exp_f32_e32 v79, v79
	v_exp_f32_e32 v80, v80
	v_mfma_f32_16x16x32_bf16 v[90:93], v[164:167], v[70:73], 0
	v_exp_f32_e32 v81, v81
	v_exp_f32_e32 v82, v82
	v_exp_f32_e32 v83, v83
	v_mfma_f32_16x16x32_bf16 v[94:97], v[168:171], v[70:73], 0
	v_exp_f32_e32 v84, v84
	v_exp_f32_e32 v85, v85
	v_exp_f32_e32 v86, v86
	v_mfma_f32_16x16x32_bf16 v[98:101], v[172:175], v[70:73], 0
	v_exp_f32_e32 v87, v87
	v_exp_f32_e32 v88, v88
	v_exp_f32_e32 v89, v89
	v_mfma_f32_16x16x32_bf16 v[102:105], v[176:179], v[70:73], 0
	v_exp_f32_e32 v90, v90
	v_exp_f32_e32 v91, v91
	v_exp_f32_e32 v92, v92
	v_mfma_f32_16x16x32_bf16 v[108:111], v[180:183], v[70:73], 0
	v_exp_f32_e32 v93, v93
	v_exp_f32_e32 v94, v94
	v_exp_f32_e32 v95, v95
	v_mfma_f32_16x16x32_bf16 v[112:115], v[184:187], v[70:73], 0
	v_exp_f32_e32 v96, v96
	v_exp_f32_e32 v97, v97
	v_exp_f32_e32 v98, v98
	v_mfma_f32_16x16x32_bf16 v[116:119], v[188:191], v[70:73], 0
	v_exp_f32_e32 v99, v99
	v_exp_f32_e32 v100, v100
	v_exp_f32_e32 v101, v101
	v_mfma_f32_16x16x32_bf16 v[120:123], v[232:235], v[70:73], 0
	v_exp_f32_e32 v102, v102
	v_exp_f32_e32 v103, v103
	v_exp_f32_e32 v104, v104
	v_mfma_f32_16x16x32_bf16 v[124:127], v[236:239], v[70:73], 0
	v_exp_f32_e32 v105, v105
	v_exp_f32_e32 v108, v108
	v_exp_f32_e32 v109, v109
	v_mfma_f32_16x16x32_bf16 v[128:131], v[240:243], v[70:73], 0
	v_exp_f32_e32 v110, v110
	v_exp_f32_e32 v111, v111
	v_exp_f32_e32 v112, v112
	v_mfma_f32_16x16x32_bf16 v[70:73], v[244:247], v[70:73], 0
	v_exp_f32_e32 v113, v113
	v_exp_f32_e32 v114, v114
	v_exp_f32_e32 v115, v115
	v_exp_f32_e32 v116, v116
	v_exp_f32_e32 v117, v117
	v_exp_f32_e32 v118, v118
	v_exp_f32_e32 v119, v119
	v_exp_f32_e32 v120, v120
	v_exp_f32_e32 v121, v121
	v_exp_f32_e32 v122, v122
	v_exp_f32_e32 v123, v123
	v_exp_f32_e32 v124, v124
	v_exp_f32_e32 v125, v125
	v_exp_f32_e32 v126, v126
	v_exp_f32_e32 v127, v127
	v_exp_f32_e32 v128, v128
	v_exp_f32_e32 v129, v129
	v_exp_f32_e32 v130, v130
	v_exp_f32_e32 v131, v131
	v_exp_f32_e32 v70, v70
	v_exp_f32_e32 v71, v71
	v_exp_f32_e32 v72, v72
	v_exp_f32_e32 v73, v73
	v_pk_add_f32 v[66:67], v[66:67], 1.0 op_sel_hi:[1,0]
	v_pk_add_f32 v[68:69], v[68:69], 1.0 op_sel_hi:[1,0]
	v_pk_add_f32 v[74:75], v[74:75], 1.0 op_sel_hi:[1,0]
	v_pk_add_f32 v[76:77], v[76:77], 1.0 op_sel_hi:[1,0]
	v_pk_add_f32 v[78:79], v[78:79], 1.0 op_sel_hi:[1,0]
	v_pk_add_f32 v[80:81], v[80:81], 1.0 op_sel_hi:[1,0]
	v_pk_add_f32 v[82:83], v[82:83], 1.0 op_sel_hi:[1,0]
	v_pk_add_f32 v[84:85], v[84:85], 1.0 op_sel_hi:[1,0]
	v_pk_add_f32 v[86:87], v[86:87], 1.0 op_sel_hi:[1,0]
	v_pk_add_f32 v[88:89], v[88:89], 1.0 op_sel_hi:[1,0]
	v_pk_add_f32 v[90:91], v[90:91], 1.0 op_sel_hi:[1,0]
	v_pk_add_f32 v[92:93], v[92:93], 1.0 op_sel_hi:[1,0]
	v_pk_add_f32 v[94:95], v[94:95], 1.0 op_sel_hi:[1,0]
	v_pk_add_f32 v[96:97], v[96:97], 1.0 op_sel_hi:[1,0]
	v_pk_add_f32 v[98:99], v[98:99], 1.0 op_sel_hi:[1,0]
	v_pk_add_f32 v[100:101], v[100:101], 1.0 op_sel_hi:[1,0]
	v_pk_add_f32 v[102:103], v[102:103], 1.0 op_sel_hi:[1,0]
	v_pk_add_f32 v[104:105], v[104:105], 1.0 op_sel_hi:[1,0]
	v_rcp_f32_e32 v66, v66
	v_rcp_f32_e32 v67, v67
	v_rcp_f32_e32 v68, v68
	v_rcp_f32_e32 v69, v69
	v_pk_add_f32 v[108:109], v[108:109], 1.0 op_sel_hi:[1,0]
	v_pk_add_f32 v[110:111], v[110:111], 1.0 op_sel_hi:[1,0]
	v_pk_add_f32 v[112:113], v[112:113], 1.0 op_sel_hi:[1,0]
	v_pk_add_f32 v[114:115], v[114:115], 1.0 op_sel_hi:[1,0]
	v_pk_add_f32 v[116:117], v[116:117], 1.0 op_sel_hi:[1,0]
	v_pk_add_f32 v[118:119], v[118:119], 1.0 op_sel_hi:[1,0]
	v_pk_add_f32 v[120:121], v[120:121], 1.0 op_sel_hi:[1,0]
	v_pk_add_f32 v[122:123], v[122:123], 1.0 op_sel_hi:[1,0]
	v_pk_add_f32 v[124:125], v[124:125], 1.0 op_sel_hi:[1,0]
	v_pk_add_f32 v[126:127], v[126:127], 1.0 op_sel_hi:[1,0]
	v_pk_add_f32 v[128:129], v[128:129], 1.0 op_sel_hi:[1,0]
	v_pk_add_f32 v[130:131], v[130:131], 1.0 op_sel_hi:[1,0]
	v_add_f32_e32 v140, 1.0, v70
	v_add_f32_e32 v141, 1.0, v71
	v_add_f32_e32 v142, 1.0, v72
	v_add_f32_e32 v143, 1.0, v73
	v_rcp_f32_e32 v70, v74
	v_rcp_f32_e32 v71, v75
	v_rcp_f32_e32 v72, v76
	v_rcp_f32_e32 v73, v77
	v_rcp_f32_e32 v74, v78
	v_rcp_f32_e32 v75, v79
	v_rcp_f32_e32 v76, v80
	v_rcp_f32_e32 v77, v81
	v_rcp_f32_e32 v78, v82
	v_rcp_f32_e32 v79, v83
	v_rcp_f32_e32 v80, v84
	v_rcp_f32_e32 v81, v85
	v_rcp_f32_e32 v82, v86
	v_rcp_f32_e32 v83, v87
	v_rcp_f32_e32 v84, v88
	v_rcp_f32_e32 v85, v89
	v_rcp_f32_e32 v86, v90
	v_rcp_f32_e32 v87, v91
	v_rcp_f32_e32 v88, v92
	v_rcp_f32_e32 v89, v93
	v_rcp_f32_e32 v90, v94
	v_rcp_f32_e32 v91, v95
	v_rcp_f32_e32 v92, v96
	v_rcp_f32_e32 v93, v97
	v_rcp_f32_e32 v94, v98
	v_rcp_f32_e32 v95, v99
	v_rcp_f32_e32 v96, v100
	v_rcp_f32_e32 v97, v101
	v_rcp_f32_e32 v98, v102
	v_rcp_f32_e32 v99, v103
	v_rcp_f32_e32 v100, v104
	v_rcp_f32_e32 v101, v105
	v_rcp_f32_e32 v102, v108
	v_rcp_f32_e32 v103, v109
	v_rcp_f32_e32 v104, v110
	v_rcp_f32_e32 v105, v111
	v_rcp_f32_e32 v108, v112
	v_rcp_f32_e32 v109, v113
	v_rcp_f32_e32 v110, v114
	v_rcp_f32_e32 v111, v115
	v_rcp_f32_e32 v112, v116
	v_rcp_f32_e32 v113, v117
	v_rcp_f32_e32 v114, v118
	v_rcp_f32_e32 v115, v119
	v_rcp_f32_e32 v116, v120
	v_rcp_f32_e32 v117, v121
	v_rcp_f32_e32 v118, v122
	v_rcp_f32_e32 v119, v123
	v_rcp_f32_e32 v120, v124
	v_rcp_f32_e32 v121, v125
	v_rcp_f32_e32 v122, v126
	v_rcp_f32_e32 v123, v127
	v_rcp_f32_e32 v124, v128
	v_rcp_f32_e32 v125, v129
	v_rcp_f32_e32 v126, v130
	v_rcp_f32_e32 v127, v131
	v_rcp_f32_e32 v128, v140
	v_rcp_f32_e32 v129, v141
	v_rcp_f32_e32 v130, v142
	v_rcp_f32_e32 v131, v143
	v_pk_fma_f32 v[66:67], v[66:67], -2.0, 1.0 op_sel_hi:[1,0,0]
	v_pk_fma_f32 v[68:69], v[68:69], -2.0, 1.0 op_sel_hi:[1,0,0]
	v_pk_fma_f32 v[70:71], v[70:71], -2.0, 1.0 op_sel_hi:[1,0,0]
	v_pk_fma_f32 v[72:73], v[72:73], -2.0, 1.0 op_sel_hi:[1,0,0]
	v_pk_fma_f32 v[74:75], v[74:75], -2.0, 1.0 op_sel_hi:[1,0,0]
	v_pk_fma_f32 v[76:77], v[76:77], -2.0, 1.0 op_sel_hi:[1,0,0]
	v_pk_fma_f32 v[78:79], v[78:79], -2.0, 1.0 op_sel_hi:[1,0,0]
	v_pk_fma_f32 v[80:81], v[80:81], -2.0, 1.0 op_sel_hi:[1,0,0]
	v_pk_fma_f32 v[82:83], v[82:83], -2.0, 1.0 op_sel_hi:[1,0,0]
	v_pk_fma_f32 v[84:85], v[84:85], -2.0, 1.0 op_sel_hi:[1,0,0]
	v_pk_fma_f32 v[86:87], v[86:87], -2.0, 1.0 op_sel_hi:[1,0,0]
	v_pk_fma_f32 v[88:89], v[88:89], -2.0, 1.0 op_sel_hi:[1,0,0]
	v_pk_fma_f32 v[90:91], v[90:91], -2.0, 1.0 op_sel_hi:[1,0,0]
	v_pk_fma_f32 v[92:93], v[92:93], -2.0, 1.0 op_sel_hi:[1,0,0]
	v_pk_fma_f32 v[94:95], v[94:95], -2.0, 1.0 op_sel_hi:[1,0,0]
	v_pk_fma_f32 v[96:97], v[96:97], -2.0, 1.0 op_sel_hi:[1,0,0]
	v_pk_fma_f32 v[98:99], v[98:99], -2.0, 1.0 op_sel_hi:[1,0,0]
	v_pk_fma_f32 v[100:101], v[100:101], -2.0, 1.0 op_sel_hi:[1,0,0]
	ds_write_b128 v214, v[66:69]
	ds_write_b128 v214, v[70:73] offset:64
	ds_write_b128 v214, v[74:77] offset:128
	ds_write_b128 v214, v[78:81] offset:192
	ds_write_b128 v214, v[82:85] offset:256
	ds_write_b128 v214, v[86:89] offset:320
	ds_write_b128 v214, v[90:93] offset:384
	ds_write_b128 v214, v[94:97] offset:448
	v_pk_fma_f32 v[102:103], v[102:103], -2.0, 1.0 op_sel_hi:[1,0,0]
	v_pk_fma_f32 v[104:105], v[104:105], -2.0, 1.0 op_sel_hi:[1,0,0]
	v_pk_fma_f32 v[108:109], v[108:109], -2.0, 1.0 op_sel_hi:[1,0,0]
	v_pk_fma_f32 v[110:111], v[110:111], -2.0, 1.0 op_sel_hi:[1,0,0]
	v_pk_fma_f32 v[112:113], v[112:113], -2.0, 1.0 op_sel_hi:[1,0,0]
	v_pk_fma_f32 v[114:115], v[114:115], -2.0, 1.0 op_sel_hi:[1,0,0]
	v_pk_fma_f32 v[116:117], v[116:117], -2.0, 1.0 op_sel_hi:[1,0,0]
	v_pk_fma_f32 v[118:119], v[118:119], -2.0, 1.0 op_sel_hi:[1,0,0]
	v_pk_fma_f32 v[120:121], v[120:121], -2.0, 1.0 op_sel_hi:[1,0,0]
	v_pk_fma_f32 v[122:123], v[122:123], -2.0, 1.0 op_sel_hi:[1,0,0]
	v_pk_fma_f32 v[124:125], v[124:125], -2.0, 1.0 op_sel_hi:[1,0,0]
	v_pk_fma_f32 v[126:127], v[126:127], -2.0, 1.0 op_sel_hi:[1,0,0]
	v_pk_fma_f32 v[128:129], v[128:129], -2.0, 1.0 op_sel_hi:[1,0,0]
	v_pk_fma_f32 v[130:131], v[130:131], -2.0, 1.0 op_sel_hi:[1,0,0]
	ds_read_b128 v[66:69], v215
	ds_read_b128 v[70:73], v215 offset:1056
	ds_read_b128 v[74:77], v215 offset:2112
	ds_read_b128 v[78:81], v215 offset:3168
	ds_read_b128 v[82:85], v215 offset:4224
	ds_read_b128 v[86:89], v215 offset:5280
	ds_read_b128 v[90:93], v215 offset:6336
	ds_read_b128 v[94:97], v215 offset:7392
	ds_write_b128 v214, v[98:101]
	ds_write_b128 v214, v[102:105] offset:64
	ds_write_b128 v214, v[108:111] offset:128
	ds_write_b128 v214, v[112:115] offset:192
	ds_write_b128 v214, v[116:119] offset:256
	ds_write_b128 v214, v[120:123] offset:320
	ds_write_b128 v214, v[124:127] offset:384
	ds_write_b128 v214, v[128:131] offset:448
	ds_read_b128 v[98:101], v215
	ds_read_b128 v[102:105], v215 offset:1056
	ds_read_b128 v[108:111], v215 offset:2112
	ds_read_b128 v[112:115], v215 offset:3168
	ds_read_b128 v[116:119], v215 offset:4224
	ds_read_b128 v[120:123], v215 offset:5280
	ds_read_b128 v[124:127], v215 offset:6336
	ds_read_b128 v[128:131], v215 offset:7392
	v_add_u32_e32 v137, 0x14000, v132
	v_add_u32_e32 v138, 0x18000, v132
	v_add_u32_e32 v139, 0x1c000, v132
	s_waitcnt lgkmcnt(14)
	buffer_store_dwordx4 v[66:69], v132, s[8:11], 0 offen sc0 nt sc1
	buffer_store_dwordx4 v[70:73], v133, s[8:11], 0 offen sc0 nt sc1
	buffer_store_dwordx4 v[74:77], v134, s[8:11], 0 offen sc0 nt sc1
	buffer_store_dwordx4 v[78:81], v135, s[8:11], 0 offen sc0 nt sc1
	buffer_store_dwordx4 v[82:85], v136, s[8:11], 0 offen sc0 nt sc1
	buffer_store_dwordx4 v[86:89], v137, s[8:11], 0 offen sc0 nt sc1
	buffer_store_dwordx4 v[90:93], v138, s[8:11], 0 offen sc0 nt sc1
	buffer_store_dwordx4 v[94:97], v139, s[8:11], 0 offen sc0 nt sc1
	s_waitcnt lgkmcnt(7)
	buffer_store_dwordx4 v[98:101], v132, s[8:11], 0 offen offset:512 sc0 nt sc1
	s_waitcnt lgkmcnt(6)
	buffer_store_dwordx4 v[102:105], v133, s[8:11], 0 offen offset:512 sc0 nt sc1
	s_waitcnt lgkmcnt(5)
	buffer_store_dwordx4 v[108:111], v134, s[8:11], 0 offen offset:512 sc0 nt sc1
	s_waitcnt lgkmcnt(4)
	buffer_store_dwordx4 v[112:115], v135, s[8:11], 0 offen offset:512 sc0 nt sc1
	s_waitcnt lgkmcnt(3)
	buffer_store_dwordx4 v[116:119], v136, s[8:11], 0 offen offset:512 sc0 nt sc1
	s_waitcnt lgkmcnt(2)
	buffer_store_dwordx4 v[120:123], v137, s[8:11], 0 offen offset:512 sc0 nt sc1
	s_waitcnt lgkmcnt(1)
	buffer_store_dwordx4 v[124:127], v138, s[8:11], 0 offen offset:512 sc0 nt sc1
	s_waitcnt lgkmcnt(0)
	buffer_store_dwordx4 v[128:131], v139, s[8:11], 0 offen offset:512 sc0 nt sc1
	s_cbranch_scc0 .LBB0_3
	s_endpgm
